# t0 scalar load moved from the scores phase into phase 1
# speedup vs baseline: 1.0096x; 1.0096x over previous
_Z7na_mainPKDF16_PKhS0_PKfS4_S4_S4_Pf:
	s_lshl_b32 s3, s2, 5
	s_and_b32 s3, s3, 0xe0
	s_ashr_i32 s2, s2, 3
	s_add_i32 s3, s3, s2
	s_ashr_i32 s2, s3, 6
	s_lshl_b32 s3, s3, 5
	s_and_b32 s14, s3, 0x7e0
	v_mov_b32_e32 v1, 0x7c0
	s_load_dwordx8 s[4:11], s[0:1], 0x0
	s_load_dwordx2 s[18:19], s[0:1], 0x20
	v_med3_u32 v1, s14, 32, v1
	v_subrev_u32_e32 v97, 32, v1
	s_ashr_i32 s3, s2, 31
	v_lshlrev_b32_e32 v58, 1, v97
	s_lshl_b64 s[12:13], s[2:3], 12
	v_mov_b32_e32 v59, 0
	v_sub_u32_e32 v60, s14, v97
	v_lshl_add_u64 v[10:11], s[12:13], 0, v[58:59]
	v_lshlrev_b64 v[2:3], 9, v[10:11]
	v_lshl_or_b32 v22, v60, 6, v0
	s_waitcnt lgkmcnt(0)
	v_and_b32_e32 v208, 31, v0
	v_lshlrev_b32_e32 v208, 5, v208
	global_load_dwordx4 v[192:195], v208, s[18:19]
	global_load_dwordx4 v[196:199], v208, s[18:19] offset:16
	v_lshl_add_u64 v[20:21], s[4:5], 0, v[2:3]
	v_ashrrev_i32_e32 v23, 31, v22
	v_lshl_add_u64 v[2:3], v[22:23], 4, v[20:21]
	global_load_dwordx4 v[12:15], v[2:3], off
	v_or_b32_e32 v28, 0x200, v22
	v_ashrrev_i32_e32 v29, 31, v28
	v_lshl_add_u64 v[2:3], v[28:29], 4, v[20:21]
	global_load_dwordx4 v[16:19], v[2:3], off
	v_or_b32_e32 v184, 0x400, v22
	v_ashrrev_i32_e32 v185, 31, v184
	v_lshl_add_u64 v[184:185], v[184:185], 4, v[20:21]
	v_or_b32_e32 v188, 0x600, v22
	v_ashrrev_i32_e32 v189, 31, v188
	v_lshl_add_u64 v[188:189], v[188:189], 4, v[20:21]
	global_load_dwordx4 v[184:187], v[184:185], off
	global_load_dwordx4 v[188:191], v[188:189], off
	v_lshrrev_b32_e32 v99, 6, v0
	v_and_b32_e32 v98, 63, v0
	v_lshlrev_b32_e32 v118, 13, v99
	v_lshl_or_b32 v58, v98, 5, v118
	s_movk_i32 s15, 0x1000
	v_lshl_add_u64 v[24:25], s[6:7], 0, v[58:59]
	v_or_b32_e32 v32, 0x400, v22
	v_or_b32_e32 v62, 0x600, v22
	v_add_co_u32_e32 v64, vcc, s15, v24
	s_mov_b64 s[12:13], 0x1000
	s_mov_b64 s[16:17], 0x1800
	v_lshlrev_b32_e32 v72, 1, v60
	v_lshrrev_b32_e32 v23, 5, v22
	v_and_b32_e32 v34, 32, v22
	v_ashrrev_i32_e32 v33, 31, v32
	v_ashrrev_i32_e32 v63, 31, v62
	v_addc_co_u32_e32 v65, vcc, 0, v25, vcc
	global_load_dwordx4 v[6:9], v58, s[6:7] offset:16
	global_load_dwordx4 v[2:5], v58, s[6:7]
	global_load_dwordx4 v[54:57], v58, s[6:7] offset:2064
	global_load_dwordx4 v[50:53], v58, s[6:7] offset:2048
	v_lshrrev_b32_e32 v58, 6, v22
	v_bfe_u32 v73, v22, 8, 2
	v_lshl_add_u64 v[26:27], v[24:25], 0, s[12:13]
	v_lshl_add_u64 v[24:25], v[24:25], 0, s[16:17]
	v_cmp_ne_u32_e32 vcc, 0, v34
	v_sub_u32_e32 v75, v23, v72
	global_load_dwordx4 v[42:45], v[64:65], off
	global_load_dwordx4 v[46:49], v[26:27], off offset:16
	global_load_dwordx4 v[34:37], v[64:65], off offset:2048
	global_load_dwordx4 v[38:41], v[24:25], off offset:16
	v_mov_b32_e32 v61, 0x60
	v_cndmask_b32_e32 v74, 0, v61, vcc
	v_add_u32_e32 v33, v74, v58
	v_lshlrev_b32_e32 v64, 2, v33
	v_bfe_u32 v96, v0, 4, 1
	v_and_b32_e32 v100, 15, v0
	v_mov_b32_e32 v30, v59
	v_mov_b32_e32 v31, v59
	v_and_b32_e32 v64, 12, v64
	v_mul_u32_u24_e32 v29, 0xc000, v96
	v_bitop3_b32 v64, v64, v100, v73 bitop3:0x36
	v_lshl_or_b32 v64, v64, 4, v29
	v_lshlrev_b32_e32 v63, 1, v75
	v_lshl_add_u32 v33, v33, 8, v64
	v_bfe_u32 v71, v0, 1, 4
	v_and_b32_e32 v70, 32, v0
	v_lshlrev_b32_e32 v1, 3, v0
	v_lshrrev_b32_e32 v58, 1, v75
	v_and_b32_e32 v1, 8, v1
	v_add_lshl_u32 v58, v58, v70, 8
	v_lshlrev_b32_e32 v121, 3, v99
	v_bfe_u32 v101, v0, 4, 2
	v_lshlrev_b32_e32 v102, 2, v101
	v_and_b32_e32 v116, 31, v0
	v_bfe_u32 v119, v0, 5, 1
	v_lshlrev_b32_e32 v124, 1, v119
	v_lshlrev_b32_e32 v117, 8, v116
	v_lshrrev_b32_e32 v95, 4, v0
	s_movk_i32 s16, 0x60
	s_mov_b32 s17, 0xc000
	v_and_b32_e32 v211, 3, v99
	v_lshrrev_b32_e32 v212, 2, v99
	v_lshl_or_b32 v211, v211, 2, v212
	v_xor_b32_e32 v213, v100, v211
	v_mul_u32_u24_e32 v214, 0x60, v119
	v_add3_u32 v214, v214, v60, v99
	v_mul_u32_u24_e32 v215, 0xc000, v96
	v_lshl_add_u32 v214, v214, 8, v215
	v_lshl_or_b32 v220, v213, 4, v214
	v_xor_b32_e32 v221, 32, v220
	v_xor_b32_e32 v216, v71, v211
	v_lshl_add_u32 v217, v119, 5, v99
	v_lshlrev_b32_e32 v217, 8, v217
	v_lshl_or_b32 v216, v216, 4, v217
	v_or_b32_e32 v216, v216, v1
	v_add_u32_e32 v222, 0x23800, v216
	v_xor_b32_e32 v223, 32, v222
	s_waitcnt vmcnt(11)
	ds_write_b128 v220, v[12:15]
	v_fma_mix_f32 v200, v192, v12, 0 op_sel_hi:[0,1,0]
	v_fma_mix_f32 v201, v193, v12, 0 op_sel:[0,1,0] op_sel_hi:[0,1,0]
	v_cvt_f32_f16_e32 v211, v12
	v_cvt_f32_f16_sdwa v212, v12 dst_sel:DWORD dst_unused:UNUSED_PAD src0_sel:WORD_1
	v_fma_mix_f32 v200, v194, v13, v200 op_sel_hi:[0,1,0]
	v_fma_mix_f32 v201, v195, v13, v201 op_sel:[0,1,0] op_sel_hi:[0,1,0]
	v_cvt_f32_f16_e32 v213, v13
	v_cvt_f32_f16_sdwa v214, v13 dst_sel:DWORD dst_unused:UNUSED_PAD src0_sel:WORD_1
	v_fma_mix_f32 v200, v196, v14, v200 op_sel_hi:[0,1,0]
	v_fma_mix_f32 v201, v197, v14, v201 op_sel:[0,1,0] op_sel_hi:[0,1,0]
	v_cvt_f32_f16_e32 v215, v14
	v_cvt_f32_f16_sdwa v216, v14 dst_sel:DWORD dst_unused:UNUSED_PAD src0_sel:WORD_1
	v_fma_mix_f32 v200, v198, v15, v200 op_sel_hi:[0,1,0]
	v_fma_mix_f32 v201, v199, v15, v201 op_sel:[0,1,0] op_sel_hi:[0,1,0]
	v_cvt_f32_f16_e32 v217, v15
	v_cvt_f32_f16_sdwa v218, v15 dst_sel:DWORD dst_unused:UNUSED_PAD src0_sel:WORD_1
	v_cvt_pk_fp8_f32 v224, v211, v212
	v_cvt_pk_fp8_f32 v225, v215, v216
	v_cvt_pk_fp8_f32 v224, v213, v214 op_sel:[0,0,1]
	v_cvt_pk_fp8_f32 v225, v217, v218 op_sel:[0,0,1]
	s_nop 0
	ds_write_b64 v222, v[224:225]
	s_waitcnt vmcnt(10)
	ds_write_b128 v221, v[16:19] offset:2048
	v_fma_mix_f32 v202, v192, v16, 0 op_sel_hi:[0,1,0]
	v_fma_mix_f32 v203, v193, v16, 0 op_sel:[0,1,0] op_sel_hi:[0,1,0]
	v_cvt_f32_f16_e32 v211, v16
	v_cvt_f32_f16_sdwa v212, v16 dst_sel:DWORD dst_unused:UNUSED_PAD src0_sel:WORD_1
	v_fma_mix_f32 v202, v194, v17, v202 op_sel_hi:[0,1,0]
	v_fma_mix_f32 v203, v195, v17, v203 op_sel:[0,1,0] op_sel_hi:[0,1,0]
	v_cvt_f32_f16_e32 v213, v17
	v_cvt_f32_f16_sdwa v214, v17 dst_sel:DWORD dst_unused:UNUSED_PAD src0_sel:WORD_1
	v_fma_mix_f32 v202, v196, v18, v202 op_sel_hi:[0,1,0]
	v_fma_mix_f32 v203, v197, v18, v203 op_sel:[0,1,0] op_sel_hi:[0,1,0]
	v_cvt_f32_f16_e32 v215, v18
	v_cvt_f32_f16_sdwa v216, v18 dst_sel:DWORD dst_unused:UNUSED_PAD src0_sel:WORD_1
	v_fma_mix_f32 v202, v198, v19, v202 op_sel_hi:[0,1,0]
	v_fma_mix_f32 v203, v199, v19, v203 op_sel:[0,1,0] op_sel_hi:[0,1,0]
	v_cvt_f32_f16_e32 v217, v19
	v_cvt_f32_f16_sdwa v218, v19 dst_sel:DWORD dst_unused:UNUSED_PAD src0_sel:WORD_1
	v_cvt_pk_fp8_f32 v226, v211, v212
	v_cvt_pk_fp8_f32 v227, v215, v216
	v_cvt_pk_fp8_f32 v226, v213, v214 op_sel:[0,0,1]
	v_cvt_pk_fp8_f32 v227, v217, v218 op_sel:[0,0,1]
	s_nop 0
	ds_write_b64 v223, v[226:227] offset:2048
	s_waitcnt vmcnt(9)
	ds_write_b128 v220, v[184:187] offset:4096
	v_fma_mix_f32 v204, v192, v184, 0 op_sel_hi:[0,1,0]
	v_fma_mix_f32 v205, v193, v184, 0 op_sel:[0,1,0] op_sel_hi:[0,1,0]
	v_cvt_f32_f16_e32 v211, v184
	v_cvt_f32_f16_sdwa v212, v184 dst_sel:DWORD dst_unused:UNUSED_PAD src0_sel:WORD_1
	v_fma_mix_f32 v204, v194, v185, v204 op_sel_hi:[0,1,0]
	v_fma_mix_f32 v205, v195, v185, v205 op_sel:[0,1,0] op_sel_hi:[0,1,0]
	v_cvt_f32_f16_e32 v213, v185
	v_cvt_f32_f16_sdwa v214, v185 dst_sel:DWORD dst_unused:UNUSED_PAD src0_sel:WORD_1
	v_fma_mix_f32 v204, v196, v186, v204 op_sel_hi:[0,1,0]
	v_fma_mix_f32 v205, v197, v186, v205 op_sel:[0,1,0] op_sel_hi:[0,1,0]
	v_cvt_f32_f16_e32 v215, v186
	v_cvt_f32_f16_sdwa v216, v186 dst_sel:DWORD dst_unused:UNUSED_PAD src0_sel:WORD_1
	v_fma_mix_f32 v204, v198, v187, v204 op_sel_hi:[0,1,0]
	v_fma_mix_f32 v205, v199, v187, v205 op_sel:[0,1,0] op_sel_hi:[0,1,0]
	v_cvt_f32_f16_e32 v217, v187
	v_cvt_f32_f16_sdwa v218, v187 dst_sel:DWORD dst_unused:UNUSED_PAD src0_sel:WORD_1
	v_cvt_pk_fp8_f32 v228, v211, v212
	v_cvt_pk_fp8_f32 v229, v215, v216
	v_cvt_pk_fp8_f32 v228, v213, v214 op_sel:[0,0,1]
	v_cvt_pk_fp8_f32 v229, v217, v218 op_sel:[0,0,1]
	s_nop 0
	ds_write_b64 v222, v[228:229] offset:4096
	s_waitcnt vmcnt(8)
	ds_write_b128 v221, v[188:191] offset:6144
	v_fma_mix_f32 v206, v192, v188, 0 op_sel_hi:[0,1,0]
	v_fma_mix_f32 v207, v193, v188, 0 op_sel:[0,1,0] op_sel_hi:[0,1,0]
	v_cvt_f32_f16_e32 v211, v188
	v_cvt_f32_f16_sdwa v212, v188 dst_sel:DWORD dst_unused:UNUSED_PAD src0_sel:WORD_1
	v_fma_mix_f32 v206, v194, v189, v206 op_sel_hi:[0,1,0]
	v_fma_mix_f32 v207, v195, v189, v207 op_sel:[0,1,0] op_sel_hi:[0,1,0]
	v_cvt_f32_f16_e32 v213, v189
	v_cvt_f32_f16_sdwa v214, v189 dst_sel:DWORD dst_unused:UNUSED_PAD src0_sel:WORD_1
	v_fma_mix_f32 v206, v196, v190, v206 op_sel_hi:[0,1,0]
	v_fma_mix_f32 v207, v197, v190, v207 op_sel:[0,1,0] op_sel_hi:[0,1,0]
	v_cvt_f32_f16_e32 v215, v190
	v_cvt_f32_f16_sdwa v216, v190 dst_sel:DWORD dst_unused:UNUSED_PAD src0_sel:WORD_1
	v_fma_mix_f32 v206, v198, v191, v206 op_sel_hi:[0,1,0]
	v_fma_mix_f32 v207, v199, v191, v207 op_sel:[0,1,0] op_sel_hi:[0,1,0]
	v_cvt_f32_f16_e32 v217, v191
	v_cvt_f32_f16_sdwa v218, v191 dst_sel:DWORD dst_unused:UNUSED_PAD src0_sel:WORD_1
	v_cvt_pk_fp8_f32 v230, v211, v212
	v_cvt_pk_fp8_f32 v231, v215, v216
	v_cvt_pk_fp8_f32 v230, v213, v214 op_sel:[0,0,1]
	v_cvt_pk_fp8_f32 v231, v217, v218 op_sel:[0,0,1]
	s_nop 0
	ds_write_b64 v223, v[230:231] offset:6144
	v_add_f32_e32 v200, v200, v201
	v_add_f32_e32 v202, v202, v203
	v_add_f32_e32 v204, v204, v205
	v_add_f32_e32 v206, v206, v207
	v_lshlrev_b32_e32 v208, 7, v119
	v_lshl_add_u32 v208, v99, 2, v208
	v_add_u32_e32 v208, 0x27800, v208
	v_add_f32_dpp v200, v200, v200 quad_perm:[1,0,3,2] row_mask:0xf bank_mask:0xf
	v_add_f32_dpp v202, v202, v202 quad_perm:[1,0,3,2] row_mask:0xf bank_mask:0xf
	v_add_f32_dpp v204, v204, v204 quad_perm:[1,0,3,2] row_mask:0xf bank_mask:0xf
	v_add_f32_dpp v206, v206, v206 quad_perm:[1,0,3,2] row_mask:0xf bank_mask:0xf
	v_add_f32_dpp v200, v200, v200 quad_perm:[2,3,0,1] row_mask:0xf bank_mask:0xf
	v_add_f32_dpp v202, v202, v202 quad_perm:[2,3,0,1] row_mask:0xf bank_mask:0xf
	v_add_f32_dpp v204, v204, v204 quad_perm:[2,3,0,1] row_mask:0xf bank_mask:0xf
	v_add_f32_dpp v206, v206, v206 quad_perm:[2,3,0,1] row_mask:0xf bank_mask:0xf
	v_add_f32_dpp v200, v200, v200 row_half_mirror row_mask:0xf bank_mask:0xf
	v_add_f32_dpp v202, v202, v202 row_half_mirror row_mask:0xf bank_mask:0xf
	v_add_f32_dpp v204, v204, v204 row_half_mirror row_mask:0xf bank_mask:0xf
	v_add_f32_dpp v206, v206, v206 row_half_mirror row_mask:0xf bank_mask:0xf
	v_add_f32_dpp v200, v200, v200 row_mirror row_mask:0xf bank_mask:0xf
	v_add_f32_dpp v202, v202, v202 row_mirror row_mask:0xf bank_mask:0xf
	v_add_f32_dpp v204, v204, v204 row_mirror row_mask:0xf bank_mask:0xf
	v_add_f32_dpp v206, v206, v206 row_mirror row_mask:0xf bank_mask:0xf
	v_add_f32_dpp v200, v200, v200 row_bcast:15 row_mask:0xa bank_mask:0xf
	v_add_f32_dpp v202, v202, v202 row_bcast:15 row_mask:0xa bank_mask:0xf
	v_add_f32_dpp v204, v204, v204 row_bcast:15 row_mask:0xa bank_mask:0xf
	v_add_f32_dpp v206, v206, v206 row_bcast:15 row_mask:0xa bank_mask:0xf
	s_mov_b32 exec_lo, 0xffff0000
	s_mov_b32 exec_hi, 0xffff0000
	ds_write_b32 v208, v200
	ds_write_b32 v208, v202 offset:32
	ds_write_b32 v208, v204 offset:64
	ds_write_b32 v208, v206 offset:96
	s_mov_b64 exec, -1
	v_lshlrev_b32_e32 v201, 7, v99
	v_lshl_or_b32 v201, v119, 4, v201
	global_load_dwordx4 v[184:187], v201, s[10:11]
	global_load_dwordx4 v[188:191], v201, s[10:11] offset:32
	global_load_dwordx4 v[192:195], v201, s[10:11] offset:64
	global_load_dwordx4 v[196:199], v201, s[10:11] offset:96
	v_cmp_lt_i32_e32 vcc, v121, v60
	s_nop 0
	v_mov_b32_e32 v15, v59
	v_cndmask_b32_e64 v12, 32, 0, vcc
	v_add_u32_e32 v16, v12, v121
	v_or_b32_e32 v12, v16, v101
	v_lshlrev_b32_e32 v58, 1, v12
	v_lshrrev_b32_e32 v12, 5, v0
	v_and_b32_e32 v12, 2, v12
	v_bitop3_b32 v14, v102, v100, v12 bitop3:0x36
	v_lshl_add_u64 v[12:13], v[10:11], 0, v[58:59]
	v_lshlrev_b64 v[12:13], 9, v[12:13]
	v_lshlrev_b32_e32 v16, 8, v16
	v_lshl_add_u64 v[12:13], s[4:5], 0, v[12:13]
	v_lshlrev_b32_e32 v14, 4, v14
	v_readfirstlane_b32 s6, v16
	v_add_u32_e32 v17, 0xc000, v16
	v_lshl_add_u64 v[12:13], v[12:13], 0, v[14:15]
	s_mov_b32 m0, s6
	s_mov_b64 s[6:7], 0x100
	v_readfirstlane_b32 s12, v17
	global_load_lds_dwordx4 v[12:13], off
	v_lshl_add_u64 v[12:13], v[12:13], 0, s[6:7]
	s_mov_b32 m0, s12
	v_or_b32_e32 v58, 1, v58
	global_load_lds_dwordx4 v[12:13], off
	v_lshl_add_u64 v[12:13], v[10:11], 0, v[58:59]
	v_lshlrev_b64 v[12:13], 9, v[12:13]
	v_lshl_add_u64 v[12:13], s[4:5], 0, v[12:13]
	v_lshl_add_u64 v[12:13], v[12:13], 0, v[14:15]
	v_add_u32_e32 v14, 0x6000, v16
	v_bfe_u32 v61, v0, 2, 2
	v_readfirstlane_b32 s12, v14
	v_add_u32_e32 v14, 0x12000, v16
	s_mov_b32 m0, s12
	v_readfirstlane_b32 s12, v14
	global_load_lds_dwordx4 v[12:13], off
	v_lshl_add_u64 v[12:13], v[12:13], 0, s[6:7]
	s_mov_b32 m0, s12
	v_add_u32_e32 v18, 0x23800, v117
	global_load_lds_dwordx4 v[12:13], off
	v_or_b32_e32 v12, 4, v121
	v_cmp_lt_i32_e32 vcc, v12, v60
	s_nop 1
	v_cndmask_b32_e64 v13, 32, 0, vcc
	v_add_u32_e32 v16, v13, v12
	v_or_b32_e32 v13, v16, v101
	v_lshlrev_b32_e32 v58, 1, v13
	v_bfe_u32 v12, v12, 2, 2
	v_bitop3_b32 v14, v102, v100, v12 bitop3:0x36
	v_lshl_add_u64 v[12:13], v[10:11], 0, v[58:59]
	v_lshlrev_b64 v[12:13], 9, v[12:13]
	v_lshlrev_b32_e32 v16, 8, v16
	v_lshl_add_u64 v[12:13], s[4:5], 0, v[12:13]
	v_lshlrev_b32_e32 v14, 4, v14
	v_readfirstlane_b32 s12, v16
	v_add_u32_e32 v17, 0xc000, v16
	v_lshl_add_u64 v[12:13], v[12:13], 0, v[14:15]
	s_mov_b32 m0, s12
	v_readfirstlane_b32 s12, v17
	v_or_b32_e32 v58, 1, v58
	global_load_lds_dwordx4 v[12:13], off
	v_lshl_add_u64 v[12:13], v[12:13], 0, s[6:7]
	s_mov_b32 m0, s12
	v_lshl_add_u64 v[10:11], v[10:11], 0, v[58:59]
	global_load_lds_dwordx4 v[12:13], off
	v_lshlrev_b64 v[10:11], 9, v[10:11]
	v_add_u32_e32 v12, 0x6000, v16
	v_lshl_add_u64 v[10:11], s[4:5], 0, v[10:11]
	v_readfirstlane_b32 s4, v12
	v_add_u32_e32 v12, 0x12000, v16
	v_lshl_add_u64 v[10:11], v[10:11], 0, v[14:15]
	s_mov_b32 m0, s4
	v_readfirstlane_b32 s4, v12
	global_load_lds_dwordx4 v[10:11], off
	v_lshl_add_u64 v[10:11], v[10:11], 0, s[6:7]
	s_mov_b32 m0, s4
	s_nop 0
	global_load_lds_dwordx4 v[10:11], off
	s_waitcnt lgkmcnt(0)
	s_barrier
	v_lshlrev_b32_e32 v10, 2, v0
	v_and_b32_e32 v94, 12, v10
	v_or_b32_e32 v120, v94, v61
	v_bitop3_b32 v10, v124, v94, v61 bitop3:0x1e
	v_lshl_or_b32 v14, v10, 4, v18
	v_bitop3_b32 v10, v124, v120, 1 bitop3:0x36
	v_lshl_or_b32 v19, v10, 4, v18
	s_load_dwordx4 s[4:7], s[0:1], 0x20
	s_load_dwordx2 s[12:13], s[0:1], 0x38
	ds_read_b128 v[10:13], v14
	ds_read_b128 v[62:65], v14 offset:8192
	ds_read_b128 v[14:17], v19
	ds_read_b128 v[66:69], v19 offset:8192
	v_bitop3_b32 v19, v124, v120, 4 bitop3:0x36
	v_lshl_or_b32 v19, v19, 4, v18
	v_bitop3_b32 v20, v124, v120, 5 bitop3:0x36
	v_lshl_or_b32 v20, v20, 4, v18
	ds_read_b128 v[70:73], v19
	ds_read_b128 v[78:81], v19 offset:8192
	ds_read_b128 v[74:77], v20
	ds_read_b128 v[82:85], v20 offset:8192
	v_bitop3_b32 v19, v124, v120, 8 bitop3:0x36
	v_lshl_or_b32 v19, v19, 4, v18
	v_bitop3_b32 v20, v124, v120, 9 bitop3:0x36
	v_lshl_or_b32 v20, v20, 4, v18
	ds_read_b128 v[86:89], v19
	ds_read_b128 v[104:107], v19 offset:8192
	ds_read_b128 v[90:93], v20
	ds_read_b128 v[108:111], v20 offset:8192
	v_bitop3_b32 v19, v124, v120, 12 bitop3:0x36
	v_lshl_or_b32 v19, v19, 4, v18
	v_bitop3_b32 v20, v124, v120, 13 bitop3:0x36
	v_lshl_or_b32 v18, v20, 4, v18
	ds_read_b128 v[126:129], v19
	ds_read_b128 v[134:137], v19 offset:8192
	ds_read_b128 v[130:133], v18
	ds_read_b128 v[138:141], v18 offset:8192
	v_mov_b32_e32 v103, 0x7f
	v_lshlrev_b32_e32 v58, 7, v99
	v_or_b32_e32 v122, 0x18000, v117
	s_waitcnt vmcnt(18) lgkmcnt(0)
	s_load_dword s4, s[6:7], 0x0
	v_mfma_scale_f32_32x32x64_f8f6f4 v[18:33], v[2:9], v[10:17], 0, v103, v103 op_sel_hi:[0,0,0]
	v_lshlrev_b32_e32 v125, 3, v119
	v_or_b32_e32 v123, 0x1a000, v117
	v_mfma_scale_f32_32x32x64_f8f6f4 v[2:17], v[2:9], v[62:69], 0, v103, v103 op_sel_hi:[0,0,0]
	v_and_b32_e32 v62, 12, v95
	s_waitcnt vmcnt(16)
	v_mfma_scale_f32_32x32x64_f8f6f4 v[18:33], v[50:57], v[70:77], v[18:33], v103, v103 op_sel_hi:[0,0,0]
	v_mfma_scale_f32_32x32x64_f8f6f4 v[2:17], v[50:57], v[78:85], v[2:17], v103, v103 op_sel_hi:[0,0,0]
	s_brev_b32 s10, 60
	v_lshlrev_b32_e32 v58, 6, v0
	v_and_b32_e32 v58, 0x4000, v58
	v_or3_b32 v63, v122, v58, v125
	v_or3_b32 v58, v123, v58, v125
	s_waitcnt vmcnt(14)
	v_mfma_scale_f32_32x32x64_f8f6f4 v[18:33], v[42:49], v[86:93], v[18:33], v103, v103 op_sel_hi:[0,0,0]
	v_mfma_scale_f32_32x32x64_f8f6f4 v[2:17], v[42:49], v[104:111], v[2:17], v103, v103 op_sel_hi:[0,0,0]
	s_nop 0
	s_waitcnt vmcnt(12)
	v_mfma_scale_f32_32x32x64_f8f6f4 v[2:17], v[34:41], v[134:141], v[2:17], v103, v103 op_sel_hi:[0,0,0]
	v_mfma_scale_f32_32x32x64_f8f6f4 v[18:33], v[34:41], v[126:133], v[18:33], v103, v103 op_sel_hi:[0,0,0]
	s_waitcnt vmcnt(8)
	s_nop 15
	s_nop 1
	v_fma_f32 v2, v2, s10, v184
	v_fma_f32 v3, v3, s10, v185
	v_fma_f32 v4, v4, s10, v186
	v_fma_f32 v5, v5, s10, v187
	v_cvt_pk_f16_f32 v2, v2, v3
	v_cvt_pk_f16_f32 v3, v4, v5
	v_bitop3_b32 v4, v95, v120, 12 bitop3:0x6c
	v_pk_fma_f32 v[18:19], v[18:19], s[10:11], v[184:185] op_sel_hi:[1,0,1]
	v_pk_fma_f32 v[20:21], v[20:21], s[10:11], v[186:187] op_sel_hi:[1,0,1]
	v_lshlrev_b32_e32 v4, 4, v4
	v_cvt_pk_f16_f32 v18, v18, v19
	v_cvt_pk_f16_f32 v19, v20, v21
	v_or_b32_e32 v5, v63, v4
	v_or_b32_e32 v4, v58, v4
	ds_write_b64 v5, v[18:19]
	ds_write_b64 v4, v[2:3]
	v_pk_fma_f32 v[2:3], v[22:23], s[10:11], v[188:189] op_sel_hi:[1,0,1]
	v_pk_fma_f32 v[4:5], v[6:7], s[10:11], v[188:189] op_sel_hi:[1,0,1]
	v_pk_fma_f32 v[6:7], v[24:25], s[10:11], v[190:191] op_sel_hi:[1,0,1]
	v_cvt_pk_f16_f32 v2, v2, v3
	v_cvt_pk_f16_f32 v3, v6, v7
	v_pk_fma_f32 v[6:7], v[8:9], s[10:11], v[190:191] op_sel_hi:[1,0,1]
	v_cvt_pk_f16_f32 v4, v4, v5
	v_cvt_pk_f16_f32 v5, v6, v7
	v_bitop3_b32 v6, v62, v120, 1 bitop3:0x36
	v_lshlrev_b32_e32 v6, 4, v6
	v_or_b32_e32 v7, v63, v6
	ds_write_b64 v7, v[2:3]
	v_or_b32_e32 v2, v58, v6
	ds_write_b64 v2, v[4:5]
	v_pk_fma_f32 v[2:3], v[26:27], s[10:11], v[192:193] op_sel_hi:[1,0,1]
	v_pk_fma_f32 v[6:7], v[28:29], s[10:11], v[194:195] op_sel_hi:[1,0,1]
	v_cvt_pk_f16_f32 v2, v2, v3
	v_pk_fma_f32 v[4:5], v[10:11], s[10:11], v[192:193] op_sel_hi:[1,0,1]
	v_cvt_pk_f16_f32 v3, v6, v7
	v_pk_fma_f32 v[6:7], v[12:13], s[10:11], v[194:195] op_sel_hi:[1,0,1]
	v_cvt_pk_f16_f32 v4, v4, v5
	v_cvt_pk_f16_f32 v5, v6, v7
	v_bitop3_b32 v6, v62, v120, 2 bitop3:0x36
	v_lshlrev_b32_e32 v6, 4, v6
	v_or_b32_e32 v7, v63, v6
	ds_write_b64 v7, v[2:3]
	v_or_b32_e32 v2, v58, v6
	ds_write_b64 v2, v[4:5]
	v_pk_fma_f32 v[2:3], v[30:31], s[10:11], v[196:197] op_sel_hi:[1,0,1]
	v_pk_fma_f32 v[6:7], v[32:33], s[10:11], v[198:199] op_sel_hi:[1,0,1]
	v_cvt_pk_f16_f32 v2, v2, v3
	v_pk_fma_f32 v[4:5], v[14:15], s[10:11], v[196:197] op_sel_hi:[1,0,1]
	v_cvt_pk_f16_f32 v3, v6, v7
	v_pk_fma_f32 v[6:7], v[16:17], s[10:11], v[198:199] op_sel_hi:[1,0,1]
	v_cvt_pk_f16_f32 v4, v4, v5
	v_cvt_pk_f16_f32 v5, v6, v7
	v_bitop3_b32 v6, v62, v120, 3 bitop3:0x36
	v_lshlrev_b32_e32 v6, 4, v6
	v_or_b32_e32 v7, v63, v6
	ds_write_b64 v7, v[2:3]
	v_or_b32_e32 v2, v58, v6
	ds_write_b64 v2, v[4:5]
	s_waitcnt vmcnt(0) lgkmcnt(0)
	s_barrier
	v_and_b32_e32 v236, 1, v101
	v_lshrrev_b32_e32 v237, 1, v101
	v_xor_b32_e32 v237, v237, v236
	v_lshl_or_b32 v236, v236, 1, v237
	v_lshrrev_b32_e32 v27, 8, v0
	v_lshrrev_b32_e32 v3, 3, v0
	v_and_b32_e32 v3, 16, v3
	v_mul_u32_u24_e32 v28, 0x60, v27
	v_lshlrev_b32_e32 v26, 5, v27
	v_or_b32_e32 v146, v3, v100
	v_or_b32_e32 v147, v28, v100
	v_or_b32_e32 v4, v146, v26
	v_lshlrev_b32_e32 v209, 2, v4
	v_add_u32_e32 v209, 0x27800, v209
	v_lshlrev_b32_e32 v4, 8, v4
	v_or_b32_e32 v5, 0x18000, v4
	v_bitop3_b32 v11, v236, v120, 12 bitop3:0x36
	v_or_b32_e32 v95, 0x1c000, v4
	v_lshlrev_b32_e32 v29, 3, v101
	v_bitop3_b32 v6, v236, v94, v61 bitop3:0x1e
	v_bitop3_b32 v8, v236, v120, 4 bitop3:0x36
	v_bitop3_b32 v10, v236, v120, 8 bitop3:0x36
	v_lshlrev_b32_e32 v94, 4, v11
	v_lshlrev_b32_e32 v6, 4, v6
	v_lshlrev_b32_e32 v8, 4, v8
	v_lshlrev_b32_e32 v58, 4, v10
	v_or_b32_e32 v7, v5, v6
	v_or_b32_e32 v9, v5, v8
	v_or_b32_e32 v10, v5, v58
	v_or_b32_e32 v5, v5, v94
	v_or_b32_e32 v6, v95, v6
	v_or_b32_e32 v60, v95, v8
	ds_read_b128 v[22:25], v7
	ds_read_b128 v[18:21], v9
	ds_read_b128 v[14:17], v10
	ds_read_b128 v[10:13], v5
	ds_read_b128 v[6:9], v6
	ds_read_b128 v[2:5], v60
	v_bfe_u32 v103, v0, 6, 1
	s_movk_i32 s5, 0x2000
	v_mad_u32_u24 v44, v103, 48, v147
	v_lshlrev_b32_e32 v60, 8, v44
	v_lshlrev_b32_e32 v44, 2, v44
	v_or_b32_e32 v35, v95, v58
	v_lshlrev_b32_e32 v58, 14, v99
	v_and_b32_e32 v44, 12, v44
	v_or_b32_e32 v56, v44, v61
	v_bitop3_b32 v44, v236, v44, v61 bitop3:0x1e
	v_lshl_add_u64 v[32:33], s[8:9], 0, v[58:59]
	v_lshlrev_b32_e32 v58, 4, v98
	v_or_b32_e32 v36, v95, v94
	v_lshl_add_u64 v[88:89], v[32:33], 0, v[58:59]
	v_lshl_or_b32 v57, v44, 4, v60
	ds_read_b128 v[40:43], v35
	ds_read_b128 v[106:109], v36
	global_load_dwordx4 v[36:39], v[88:89], off
	global_load_dwordx4 v[32:35], v[88:89], off offset:1024
	ds_read_b128 v[44:47], v57
	v_bitop3_b32 v48, v236, v56, 4 bitop3:0x36
	v_lshl_or_b32 v62, v48, 4, v60
	ds_read_b128 v[48:51], v62
	v_bitop3_b32 v52, v236, v56, 8 bitop3:0x36
	v_lshl_or_b32 v63, v52, 4, v60
	ds_read_b128 v[52:55], v63
	s_waitcnt lgkmcnt(0)
	v_mfma_f32_16x16x32_f16 v[44:47], v[44:47], v[22:25], 0
	v_bitop3_b32 v64, v236, v56, 12 bitop3:0x36
	ds_read_b128 v[56:59], v57 offset:49152
	v_lshl_or_b32 v60, v64, 4, v60
	v_mfma_f32_16x16x32_f16 v[44:47], v[48:51], v[18:21], v[44:47]
	ds_read_b128 v[68:71], v60
	ds_read_b128 v[72:75], v62 offset:49152
	v_mad_u32_u24 v104, v103, 3, 1
	v_lshlrev_b32_e32 v132, 4, v104
	v_mfma_f32_16x16x32_f16 v[44:47], v[52:55], v[14:17], v[44:47]
	v_add_u32_e32 v52, v132, v147
	global_load_dwordx4 v[64:67], v[88:89], off offset:2048
	global_load_dwordx4 v[48:51], v[88:89], off offset:3072
	ds_read_b128 v[76:79], v63 offset:49152
	ds_read_b128 v[80:83], v60 offset:49152
	s_waitcnt lgkmcnt(3)
	v_mfma_f32_16x16x32_f16 v[44:47], v[68:71], v[10:13], v[44:47]
	v_lshlrev_b32_e32 v60, 8, v52
	v_lshlrev_b32_e32 v52, 2, v52
	v_and_b32_e32 v52, 12, v52
	v_mfma_f32_16x16x32_f16 v[44:47], v[56:59], v[6:9], v[44:47]
	v_or_b32_e32 v62, v52, v61
	v_bitop3_b32 v52, v236, v52, v61 bitop3:0x1e
	v_lshl_or_b32 v63, v52, 4, v60
	s_waitcnt lgkmcnt(2)
	v_mfma_f32_16x16x32_f16 v[44:47], v[72:75], v[2:5], v[44:47]
	ds_read_b128 v[52:55], v63
	v_bitop3_b32 v56, v236, v62, 4 bitop3:0x36
	v_lshl_or_b32 v84, v56, 4, v60
	s_waitcnt lgkmcnt(2)
	v_mfma_f32_16x16x32_f16 v[44:47], v[76:79], v[40:43], v[44:47]
	ds_read_b128 v[56:59], v84
	v_bitop3_b32 v68, v236, v62, 8 bitop3:0x36
	v_lshl_or_b32 v85, v68, 4, v60
	s_waitcnt lgkmcnt(2)
	v_mfma_f32_16x16x32_f16 v[110:113], v[80:83], v[106:109], v[44:47]
	ds_read_b128 v[68:71], v63 offset:49152
	v_bitop3_b32 v62, v236, v62, 12 bitop3:0x36
	v_lshl_or_b32 v60, v62, 4, v60
	ds_read_b128 v[44:47], v85
	s_waitcnt lgkmcnt(3)
	v_mfma_f32_16x16x32_f16 v[52:55], v[52:55], v[22:25], 0
	ds_read_b128 v[72:75], v60
	ds_read_b128 v[76:79], v84 offset:49152
	v_mad_u32_u24 v105, v103, 3, 2
	v_lshlrev_b32_e32 v133, 4, v105
	s_waitcnt lgkmcnt(4)
	v_mfma_f32_16x16x32_f16 v[52:55], v[56:59], v[18:21], v[52:55]
	ds_read_b128 v[56:59], v85 offset:49152
	v_add_co_u32_e32 v114, vcc, s15, v88
	s_waitcnt lgkmcnt(3)
	v_mfma_f32_16x16x32_f16 v[44:47], v[44:47], v[14:17], v[52:55]
	v_addc_co_u32_e32 v115, vcc, 0, v89, vcc
	s_waitcnt lgkmcnt(2)
	v_mfma_f32_16x16x32_f16 v[44:47], v[72:75], v[10:13], v[44:47]
	ds_read_b128 v[52:55], v60 offset:49152
	v_add_u32_e32 v60, v133, v147
	v_lshlrev_b32_e32 v72, 8, v60
	v_lshlrev_b32_e32 v60, 2, v60
	v_mfma_f32_16x16x32_f16 v[44:47], v[68:71], v[6:9], v[44:47]
	v_and_b32_e32 v60, 12, v60
	v_or_b32_e32 v68, v60, v61
	v_bitop3_b32 v60, v236, v60, v61 bitop3:0x1e
	v_lshl_or_b32 v69, v60, 4, v72
	s_waitcnt lgkmcnt(2)
	v_mfma_f32_16x16x32_f16 v[44:47], v[76:79], v[2:5], v[44:47]
	ds_read_b128 v[60:63], v69
	v_bitop3_b32 v70, v236, v68, 4 bitop3:0x36
	v_lshl_or_b32 v70, v70, 4, v72
	s_waitcnt lgkmcnt(2)
	v_mfma_f32_16x16x32_f16 v[44:47], v[56:59], v[40:43], v[44:47]
	ds_read_b128 v[56:59], v70
	v_bitop3_b32 v71, v236, v68, 8 bitop3:0x36
	v_lshl_or_b32 v71, v71, 4, v72
	s_waitcnt lgkmcnt(1)
	v_mfma_f32_16x16x32_f16 v[22:25], v[60:63], v[22:25], 0
	v_bitop3_b32 v60, v236, v68, 12 bitop3:0x36
	v_lshl_or_b32 v68, v60, 4, v72
	ds_read_b32 v210, v209
	v_mfma_f32_16x16x32_f16 v[126:129], v[52:55], v[106:109], v[44:47]
	s_nop 2
	ds_read_b128 v[44:47], v71
	ds_read_b128 v[52:55], v69 offset:49152
	ds_read_b128 v[60:63], v70 offset:49152
	s_waitcnt lgkmcnt(4)
	v_mfma_f32_16x16x32_f16 v[18:21], v[56:59], v[18:21], v[22:25]
	ds_read_b128 v[56:59], v71 offset:49152
	s_nop 1
	ds_read_b128 v[22:25], v68
	s_waitcnt lgkmcnt(4)
	v_mfma_f32_16x16x32_f16 v[14:17], v[44:47], v[14:17], v[18:21]
	v_add_co_u32_e32 v44, vcc, s5, v88
	s_movk_i32 s5, 0x3000
	s_nop 0
	ds_read_b128 v[18:21], v68 offset:49152
	s_waitcnt lgkmcnt(1)
	v_mfma_f32_16x16x32_f16 v[10:13], v[22:25], v[10:13], v[14:17]
	v_addc_co_u32_e32 v45, vcc, 0, v89, vcc
	global_load_dwordx4 v[84:87], v[114:115], off offset:1024
	global_load_dwordx4 v[80:83], v[114:115], off offset:2048
	global_load_dwordx4 v[92:95], v[44:45], off offset:-4096
	global_load_dwordx4 v[76:79], v[44:45], off
	v_mfma_f32_16x16x32_f16 v[6:9], v[52:55], v[6:9], v[10:13]
	global_load_dwordx4 v[72:75], v[44:45], off offset:1024
	global_load_dwordx4 v[68:71], v[44:45], off offset:2048
	global_load_dwordx4 v[52:55], v[44:45], off offset:3072
	v_mov_b32_e32 v13, 0xff61b1e6
	v_mfma_f32_16x16x32_f16 v[2:5], v[60:63], v[2:5], v[6:9]
	s_nop 2
	v_add_co_u32_e32 v6, vcc, s5, v88
	v_mfma_f32_16x16x32_f16 v[2:5], v[56:59], v[40:43], v[2:5]
	s_nop 0
	v_addc_co_u32_e32 v7, vcc, 0, v89, vcc
	global_load_dwordx4 v[88:91], v[114:115], off offset:3072
	global_load_dwordx4 v[60:63], v[6:7], off
	global_load_dwordx4 v[56:59], v[6:7], off offset:1024
	global_load_dwordx4 v[44:47], v[6:7], off offset:2048
	global_load_dwordx4 v[40:43], v[6:7], off offset:3072
	s_waitcnt lgkmcnt(0)
	v_mfma_f32_16x16x32_f16 v[16:19], v[18:21], v[106:109], v[2:5]
	s_mov_b32 s5, 0xff61b1e6
	s_nop 0
	v_or_b32_e32 v3, s14, v146
	v_mov_b32_e32 v4, 0x7df
	v_med3_u32 v3, v3, 32, v4
	v_or_b32_e32 v4, v97, v102
	v_sub_u32_e32 v3, v4, v3
	v_add_f32_e32 v2, s4, v210
	v_add_u32_e32 v3, 32, v3
	v_mad_u32_u24 v4, v103, 48, v3
	s_movk_i32 s4, 0x41
	v_add_f32_e32 v5, v2, v110
	v_mul_f32_e32 v5, 0x3db8aa3b, v5
	v_cmp_gt_u32_e32 vcc, s4, v4
	v_add_u32_e32 v6, 1, v4
	v_add_f32_e32 v7, v2, v111
	v_cndmask_b32_e32 v5, v13, v5, vcc
	v_mul_f32_e32 v7, 0x3db8aa3b, v7
	v_cmp_gt_u32_e32 vcc, s4, v6
	v_add_u32_e32 v8, 2, v4
	v_add_f32_e32 v9, v2, v112
	v_cndmask_b32_e32 v6, v13, v7, vcc
	v_mul_f32_e32 v9, 0x3db8aa3b, v9
	v_cmp_gt_u32_e32 vcc, s4, v8
	v_add_u32_e32 v4, 3, v4
	v_max3_f32 v7, v5, s5, v6
	v_cndmask_b32_e32 v8, v13, v9, vcc
	v_add_f32_e32 v9, v2, v113
	v_mul_f32_e32 v9, 0x3db8aa3b, v9
	v_cmp_gt_u32_e32 vcc, s4, v4
	v_add_u32_e32 v11, v3, v132
	v_add_f32_e32 v12, v2, v127
	v_cndmask_b32_e32 v10, v13, v9, vcc
	v_max3_f32 v4, v7, v8, v10
	v_add_f32_e32 v7, v2, v126
	v_mul_f32_e32 v7, 0x3db8aa3b, v7
	v_cmp_gt_u32_e32 vcc, s4, v11
	v_add_u32_e32 v9, 1, v11
	v_mul_f32_e32 v12, 0x3db8aa3b, v12
	v_cndmask_b32_e32 v7, v13, v7, vcc
	v_cmp_gt_u32_e32 vcc, s4, v9
	v_add_f32_e32 v14, v2, v128
	v_mul_f32_e32 v14, 0x3db8aa3b, v14
	v_cndmask_b32_e32 v9, v13, v12, vcc
	v_add_u32_e32 v12, 2, v11
	v_cmp_gt_u32_e32 vcc, s4, v12
	v_add_u32_e32 v11, 3, v11
	v_add_u32_e32 v3, v3, v133
	v_cndmask_b32_e32 v12, v13, v14, vcc
	v_add_f32_e32 v14, v2, v129
	v_mul_f32_e32 v14, 0x3db8aa3b, v14
	v_cmp_gt_u32_e32 vcc, s4, v11
	v_add_f32_e32 v11, v2, v16
	v_mul_f32_e32 v11, 0x3db8aa3b, v11
	v_cndmask_b32_e32 v15, v13, v14, vcc
	v_cmp_gt_u32_e32 vcc, s4, v3
	v_add_u32_e32 v14, 1, v3
	v_add_f32_e32 v16, v2, v17
	v_cndmask_b32_e32 v11, v13, v11, vcc
	v_mul_f32_e32 v16, 0x3db8aa3b, v16
	v_cmp_gt_u32_e32 vcc, s4, v14
	v_add_f32_e32 v17, v2, v18
	v_max3_f32 v4, v4, v7, v9
	v_cndmask_b32_e32 v14, v13, v16, vcc
	v_add_u32_e32 v16, 2, v3
	v_mul_f32_e32 v17, 0x3db8aa3b, v17
	v_cmp_gt_u32_e32 vcc, s4, v16
	v_add_u32_e32 v3, 3, v3
	v_add_f32_e32 v2, v2, v19
	v_max3_f32 v4, v4, v12, v15
	v_cndmask_b32_e32 v16, v13, v17, vcc
	v_mul_f32_e32 v2, 0x3db8aa3b, v2
	v_cmp_gt_u32_e32 vcc, s4, v3
	v_max3_f32 v4, v4, v11, v14
	v_lshlrev_b32_e32 v126, 5, v99
	v_cndmask_b32_e32 v17, v13, v2, vcc
	v_max3_f32 v2, v4, v16, v17
	v_mov_b32_e32 v3, v2
	v_lshlrev_b32_e32 v127, 2, v119
	v_lshrrev_b32_e32 v4, 7, v0
	v_cmp_gt_u32_e32 vcc, 16, v98
	v_permlane16_swap_b32_e32 v3, v2
	v_max_f32_e32 v2, v2, v3
	v_mov_b32_e32 v3, v2
	s_nop 1
	v_permlane32_swap_b32_e32 v3, v2
	v_max_f32_e32 v13, v2, v3
	v_and_b32_e32 v2, 0x180, v0
	v_or_b32_e32 v2, 0x23400, v2
	v_lshlrev_b32_e32 v3, 2, v100
	s_and_saveexec_b64 s[4:5], vcc
	v_lshlrev_b32_e32 v18, 6, v103
	v_add3_u32 v18, v2, v18, v3
	ds_write_b32 v18, v13
	s_or_b64 exec, exec, s[4:5]
	v_lshlrev_b32_e32 v18, 4, v103
	v_bitop3_b32 v19, v18, 16, v100 bitop3:0x36
	v_lshl_add_u32 v2, v19, 2, v2
	s_waitcnt lgkmcnt(0)
	s_barrier
	ds_read_b32 v19, v2
	v_max_f32_e32 v13, v13, v13
	v_mul_u32_u24_e32 v20, 0xd00, v4
	s_load_dwordx2 s[0:1], s[0:1], 0x30
	v_or_b32_e32 v2, 1, v124
	s_waitcnt lgkmcnt(0)
	v_max_f32_e32 v19, v19, v19
	v_max_f32_e32 v19, v13, v19
	v_sub_f32_e32 v5, v5, v19
	v_exp_f32_e32 v5, v5
	v_sub_f32_e32 v6, v6, v19
	v_exp_f32_e32 v6, v6
	v_sub_f32_e32 v8, v8, v19
	v_mul_u32_u24_e32 v13, 0xd0, v100
	v_exp_f32_e32 v8, v8
	v_sub_f32_e32 v10, v10, v19
	v_add3_u32 v20, v13, v20, v29
	v_exp_f32_e32 v10, v10
	v_or_b32_e32 v22, 0x20000, v20
	v_add_f32_e32 v20, 0, v5
	v_add_f32_e32 v20, v20, v6
	v_add_f32_e32 v20, v20, v8
	v_add_f32_e32 v23, v20, v10
	v_cvt_pk_f16_f32 v21, v8, v10
	v_cvt_pk_f16_f32 v20, v5, v6
	v_mad_u32_u24 v5, v103, s16, v22
	ds_write_b64 v5, v[20:21]
	v_sub_f32_e32 v5, v7, v19
	v_exp_f32_e32 v5, v5
	v_sub_f32_e32 v6, v9, v19
	v_exp_f32_e32 v6, v6
	v_sub_f32_e32 v7, v12, v19
	v_exp_f32_e32 v7, v7
	v_sub_f32_e32 v8, v15, v19
	v_exp_f32_e32 v8, v8
	v_sub_f32_e32 v10, v11, v19
	v_add_f32_e32 v9, v23, v5
	v_exp_f32_e32 v10, v10
	v_sub_f32_e32 v11, v14, v19
	v_add_f32_e32 v9, v9, v6
	v_exp_f32_e32 v11, v11
	v_sub_f32_e32 v12, v16, v19
	v_add_f32_e32 v9, v9, v7
	v_exp_f32_e32 v12, v12
	v_sub_f32_e32 v14, v17, v19
	v_add_f32_e32 v9, v9, v8
	v_exp_f32_e32 v14, v14
	v_add_f32_e32 v9, v9, v10
	v_add_f32_e32 v9, v9, v11
	v_add_f32_e32 v9, v9, v12
	v_add_f32_e32 v9, v9, v14
	v_mov_b32_e32 v15, v9
	v_cvt_pk_f16_f32 v7, v7, v8
	v_cvt_pk_f16_f32 v6, v5, v6
	v_lshl_add_u32 v5, v104, 5, v22
	ds_write_b64 v5, v[6:7]
	v_permlane16_swap_b32_e32 v15, v9
	v_add_f32_e32 v5, v9, v15
	v_mov_b32_e32 v6, v5
	s_movk_i32 s7, 0xd00
	s_mov_b32 s6, 0x20000
	v_cvt_pk_f16_f32 v9, v12, v14
	v_cvt_pk_f16_f32 v8, v10, v11
	v_lshl_add_u32 v7, v105, 5, v22
	ds_write_b64 v7, v[8:9]
	v_permlane32_swap_b32_e32 v6, v5
	s_and_saveexec_b64 s[4:5], vcc
	s_cbranch_execz .LBB1_4
	v_lshlrev_b32_e32 v4, 5, v4
	v_or_b32_e32 v7, v18, v100
	v_lshlrev_b32_e32 v4, 2, v4
	v_lshlrev_b32_e32 v7, 2, v7
	s_mov_b32 s8, 0x23600
	v_add3_u32 v4, v7, v4, s8
	v_add_f32_e32 v5, v5, v6
	ds_write_b32 v4, v5
